# speedup vs baseline: 1.0211x; 1.0202x over previous
.LBB0_37:
	s_or_b64 exec, exec, s[14:15]
	s_load_dwordx4 s[52:55], s[0:1], 0x40
	s_load_dwordx2 s[14:15], s[0:1], 0x0
	s_load_dwordx2 s[22:23], s[0:1], 0x30
	s_mov_b64 vcc, s[4:5]
	v_mov_b32_e32 v4, 0
	v_cndmask_b32_e32 v7, 0, v20, vcc
	s_waitcnt vmcnt(0)
	v_mov_b32_e32 v6, 0
	s_waitcnt lgkmcnt(0)
	s_barrier
	v_cmp_gt_u32_e32 vcc, 0x80, v0
	s_and_saveexec_b64 s[64:65], vcc
	s_cbranch_execz .Lbv_ld_skip
	v_lshlrev_b32_e32 v118, 2, v0
	global_load_dword v119, v118, s[22:23]
.Lbv_ld_skip:
	s_or_b64 exec, exec, s[64:65]
	s_and_saveexec_b64 s[0:1], s[4:5]
	v_mov_b32_e32 v5, 0x1e100
	v_lshl_add_u32 v5, v7, 2, v5
	v_mov_b32_e32 v6, 1
	ds_add_rtn_u32 v6, v5, v6
	s_or_b64 exec, exec, s[0:1]
	v_mov_b32_e32 v5, 0x26500
	v_lshl_add_u32 v7, v7, 3, v5
	ds_read_b32 v8, v7
	s_mov_b64 vcc, s[6:7]
	v_cndmask_b32_e32 v7, 0, v19, vcc
	s_and_saveexec_b64 s[0:1], s[6:7]
	v_mov_b32_e32 v4, 0x1e100
	v_lshl_add_u32 v4, v7, 2, v4
	v_mov_b32_e32 v9, 1
	ds_add_rtn_u32 v4, v4, v9
	s_or_b64 exec, exec, s[0:1]
	v_lshl_add_u32 v5, v7, 3, v5
	ds_read_b32 v9, v5
	s_mov_b64 vcc, s[8:9]
	v_mov_b32_e32 v5, 0
	v_cndmask_b32_e32 v18, 0, v18, vcc
	v_mov_b32_e32 v7, 0
	s_and_saveexec_b64 s[0:1], s[8:9]
	v_mov_b32_e32 v7, 0x1e100
	v_lshl_add_u32 v7, v18, 2, v7
	v_mov_b32_e32 v19, 1
	ds_add_rtn_u32 v7, v7, v19
	s_or_b64 exec, exec, s[0:1]
	v_mov_b32_e32 v19, 0x26500
	v_lshl_add_u32 v18, v18, 3, v19
	ds_read_b32 v18, v18
	s_mov_b64 vcc, s[10:11]
	v_cndmask_b32_e32 v17, 0, v17, vcc
	s_and_saveexec_b64 s[0:1], s[10:11]
	v_mov_b32_e32 v5, 0x1e100
	v_lshl_add_u32 v5, v17, 2, v5
	v_mov_b32_e32 v20, 1
	ds_add_rtn_u32 v5, v5, v20
	s_or_b64 exec, exec, s[0:1]
	v_lshl_add_u32 v17, v17, 3, v19
	ds_read_b32 v17, v17
	s_and_saveexec_b64 s[0:1], s[4:5]
	s_cbranch_execnz .LBB0_53
	s_or_b64 exec, exec, s[0:1]
	s_and_saveexec_b64 s[0:1], s[6:7]
	s_cbranch_execnz .LBB0_54

.LBB0_67:
	s_waitcnt lgkmcnt(3)
	v_mov_b32_e32 v4, 0
	v_cmp_eq_u32_e64 s[2:3], 0, v3
	v_cmp_gt_u32_e32 vcc, 0x80, v0
	s_and_saveexec_b64 s[64:65], vcc
	s_cbranch_execz .Lbv_st_skip
	v_add_u32_e32 v118, 0x26b50, v118
	s_waitcnt vmcnt(0)
	ds_write_b32 v118, v119
.Lbv_st_skip:
	s_or_b64 exec, exec, s[64:65]
	s_waitcnt lgkmcnt(0)
	s_barrier
	s_and_saveexec_b64 s[0:1], s[2:3]
	s_cbranch_execz .LBB0_71
	s_mov_b64 s[6:7], exec
	v_mbcnt_lo_u32_b32 v4, s6, 0
	v_mbcnt_hi_u32_b32 v4, s7, v4
	v_cmp_eq_u32_e32 vcc, 0, v4
	s_and_saveexec_b64 s[4:5], vcc
	s_bcnt1_i32_b64 s6, s[6:7]
	v_mov_b32_e32 v5, 0x26b40
	v_mov_b32_e32 v6, s6
	ds_add_rtn_u32 v5, v5, v6
	s_or_b64 exec, exec, s[4:5]
	s_waitcnt lgkmcnt(0)
	v_readfirstlane_b32 s4, v5
	s_nop 1
	v_add_u32_e32 v4, s4, v4

.LBB0_89:
	s_or_b64 exec, exec, s[8:9]
	v_mov_b32_e32 v3, 0
	v_lshlrev_b32_e32 v70, 4, v28
	s_and_saveexec_b64 s[60:61], vcc
	s_cbranch_execz .LBB0_118
	s_mov_b64 s[92:93], s[14:15]
	v_lshl_add_u64 v[22:23], s[12:13], 0, v[2:3]
	s_waitcnt vmcnt(0)
	v_cndmask_b32_e64 v55, -1, v4, s[0:1]
	s_movk_i32 s0, 0x880
	v_mov_b32_e32 v2, 0x1dd00
	v_mad_u32_u24 v4, v80, s0, v2
	v_lshlrev_b32_e32 v2, 1, v1
	v_mov_b32_e32 v27, v3
	v_mbcnt_hi_u32_b32 v2, -1, v29
	v_lshl_add_u64 v[72:73], v[22:23], 0, v[26:27]
	v_and_b32_e32 v23, 64, v2
	v_xor_b32_e32 v22, 16, v2
	v_add_u32_e32 v23, 64, v23
	v_cmp_lt_i32_e32 vcc, v22, v23
	v_lshlrev_b32_e32 v88, 2, v28
	v_and_b32_e32 v24, 7, v0
	v_cndmask_b32_e32 v22, v2, v22, vcc
	v_lshlrev_b32_e32 v90, 2, v22
	v_xor_b32_e32 v22, 32, v2
	v_cmp_lt_i32_e32 vcc, v22, v23
	s_mov_b32 s24, 0x10000
	v_cndmask_b32_e32 v2, v2, v22, vcc
	v_lshlrev_b32_e32 v91, 2, v2
	v_lshrrev_b32_e32 v2, 2, v79
	v_mul_u32_u24_e32 v22, 0x88, v79
	v_add3_u32 v92, v4, v22, v1
	v_or_b32_e32 v2, v88, v2
	v_lshlrev_b32_e32 v22, 3, v0
	v_mul_u32_u24_e32 v2, 0x88, v2
	v_and_b32_e32 v22, 24, v22
	v_add3_u32 v93, v4, v2, v22
	v_lshlrev_b32_e32 v2, 5, v24
	v_or3_b32 v78, v2, v1, s24
	v_bfe_u32 v2, v0, 1, 2
	v_lshrrev_b32_e32 v89, 3, v79
	v_cmp_eq_u32_e64 s[6:7], 4, v24
	v_cmp_eq_u32_e64 s[8:9], 3, v24
	v_cmp_eq_u32_e64 s[10:11], 2, v24
	v_cmp_eq_u32_e64 s[12:13], 1, v24
	v_cmp_eq_u32_e64 s[14:15], 0, v24
	v_cmp_eq_u32_e64 s[16:17], 7, v24
	v_cmp_eq_u32_e64 s[18:19], 6, v24
	v_cmp_eq_u32_e64 s[20:21], 5, v24
	v_cmp_eq_u32_e64 s[22:23], 0, v2
	v_cmp_eq_u32_e64 s[24:25], 1, v2
	v_cmp_eq_u32_e64 s[26:27], 2, v2
	v_cmp_eq_u32_e64 s[28:29], 3, v2
	s_and_b64 s[22:23], s[22:23], s[4:5]
	s_and_b64 s[24:25], s[24:25], s[4:5]
	s_and_b64 s[26:27], s[26:27], s[4:5]
	s_and_b64 s[28:29], s[28:29], s[4:5]
	v_mov_b32_e32 v71, 0xf149f2ca
	s_mov_b64 s[62:63], 0
	s_mov_b32 s69, 0xf149f2ca
	s_mov_b32 s70, 0xefa18f08
	s_mov_b32 s71, 0x41000000
	s_movk_i32 s72, 0x110
	s_mov_b32 s77, 0x26500
	s_mov_b32 s73, 0x2650c
	s_mov_b32 s80, -1
	s_mov_b32 s81, 0
	s_mov_b32 s82, 0
	s_mov_b32 s83, 0x7fffffff
	s_mov_b64 s[84:85], 0
	v_mov_b32_e32 v100, 0
	v_mov_b32_e32 v4, 0
	v_mov_b32_e32 v103, 0xf149f2ca
	v_mov_b32_e32 v46, v3
	v_mov_b32_e32 v47, v3
	v_mov_b32_e32 v48, v3
	v_mov_b32_e32 v49, v3
	v_mov_b32_e32 v50, v3
	v_mov_b32_e32 v51, v3
	v_mov_b32_e32 v52, v3
	v_mov_b32_e32 v53, v3
	v_mov_b32_e32 v38, v3
	v_mov_b32_e32 v39, v3
	v_mov_b32_e32 v40, v3
	v_mov_b32_e32 v41, v3
	v_mov_b32_e32 v42, v3
	v_mov_b32_e32 v43, v3
	v_mov_b32_e32 v44, v3
	v_mov_b32_e32 v45, v3
	v_mov_b32_e32 v30, v3
	v_mov_b32_e32 v31, v3
	v_mov_b32_e32 v32, v3
	v_mov_b32_e32 v33, v3
	v_mov_b32_e32 v34, v3
	v_mov_b32_e32 v35, v3
	v_mov_b32_e32 v36, v3
	v_mov_b32_e32 v37, v3
	v_mov_b32_e32 v22, v3
	v_mov_b32_e32 v23, v3
	v_mov_b32_e32 v24, v3
	v_mov_b32_e32 v25, v3
	v_mov_b32_e32 v26, v3
	v_mov_b32_e32 v28, v3
	v_mov_b32_e32 v29, v3
	s_branch .LBB0_95

.LBB0_94:
	s_or_b64 exec, exec, s[0:1]
	s_waitcnt vmcnt(4)
	v_cndmask_b32_e64 v55, -1, v98, s[30:31]
	v_mov_b32_e32 v99, v83
	v_mov_b32_e32 v5, v81
	v_mov_b32_e32 v100, v84
	v_mov_b32_e32 v84, v57
	v_mov_b32_e32 v81, v56
	v_mov_b32_e32 v83, v2
	v_mov_b32_e32 v80, v87
	s_mov_b32 s80, s86
	s_mov_b32 s81, s87
	s_mov_b32 s83, s88
	s_mov_b32 s82, s89
	s_mov_b64 s[84:85], s[90:91]
	s_andn2_b64 exec, exec, s[62:63]
	s_cbranch_execz .LBB0_118
.LBB0_95:
	v_mov_b32_e32 v87, v54
	v_readfirstlane_b32 s86, v80
	v_readfirstlane_b32 s87, v100
	v_readfirstlane_b32 s88, v99
	v_readfirstlane_b32 s89, v5
	v_lshl_or_b32 v2, v84, 4, v79
	v_cmp_gt_i32_e64 s[34:35], s68, v87
	v_cmp_gt_i32_e64 s[78:79], s68, v80
	v_cmp_le_i32_e64 s[36:37], s68, v80
	v_cmp_lt_i32_e32 vcc, v2, v83
	v_add_u32_e32 v2, v2, v85
	v_ashrrev_i32_e32 v104, 31, v2
	s_and_b64 s[30:31], s[34:35], vcc
	v_cndmask_b32_e64 v109, 0, v104, s[30:31]
	v_cndmask_b32_e64 v108, 0, v2, s[30:31]
	v_lshl_add_u64 v[108:109], v[108:109], 2, s[58:59]
	v_and_b32_e32 v2, 0x10000, v55
	v_lshlrev_b32_e32 v104, 7, v55
	v_and_b32_e32 v104, 0x7fff80, v104
	v_cmp_eq_u32_e32 vcc, 0, v2
	s_mov_b64 s[90:91], vcc
	v_cndmask_b32_e32 v2, 0, v104, vcc
	v_lshl_add_u32 v2, v2, 1, v70
	s_lshl_b32 s94, s81, 4
	s_add_i32 s95, s94, 16
	s_cmp_ge_i32 s95, s83
	s_cselect_b64 s[0:1], -1, 0
	s_and_b64 s[42:43], s[78:79], s[0:1]
	s_waitcnt vmcnt(0)
	v_mov_b64_e32 v[66:67], v[74:75]
	v_mov_b64_e32 v[68:69], v[76:77]
	v_mov_b64_e32 v[62:63], v[94:95]
	v_mov_b64_e32 v[64:65], v[96:97]
	v_mov_b64_e32 v[58:59], v[120:121]
	v_mov_b64_e32 v[60:61], v[122:123]
	v_mov_b64_e32 v[54:55], v[124:125]
	v_mov_b64_e32 v[56:57], v[126:127]
	s_and_saveexec_b64 s[40:41], s[42:43]
	s_cbranch_execz .LBB0_97
	v_lshlrev_b32_e32 v99, 1, v80
	v_or_b32_e32 v100, 1, v99
	v_min_i32_e32 v100, s67, v100
	v_cndmask_b32_e64 v99, v100, v99, s[38:39]
	v_add_u32_e32 v100, s66, v99
	v_ashrrev_i32_e32 v101, 31, v100
	v_lshlrev_b64 v[100:101], 8, v[100:101]
	v_lshl_add_u64 v[100:101], v[72:73], 0, v[100:101]
	global_load_dwordx4 v[112:115], v[100:101], off nt
.LBB0_97:
	s_or_b64 exec, exec, s[40:41]
	global_load_dword v98, v[108:109], off
	global_load_dwordx4 v[74:77], v2, s[92:93]
	global_load_dwordx4 v[94:97], v2, s[92:93] offset:64
	global_load_dwordx4 v[120:123], v2, s[92:93] offset:128
	global_load_dwordx4 v[124:127], v2, s[92:93] offset:192
	s_cmp_lt_i32 s80, 0
	s_cbranch_scc1 .Lattn_skip
	v_mfma_f32_16x16x32_f16 v[104:107], v[66:69], v[6:9], 0
	v_or_b32_e32 v2, s94, v79
	v_cmp_lt_i32_e64 s[42:43], v2, s82
	v_cmp_ge_i32_e64 s[40:41], v2, s82
	v_mfma_f32_16x16x32_f16 v[104:107], v[62:65], v[10:13], v[104:107]
	s_and_b64 s[42:43], s[84:85], s[42:43]
	v_cndmask_b32_e64 v2, 0, 1, s[42:43]
	s_and_b64 s[40:41], s[40:41], s[84:85]
	v_cmp_ne_u32_e64 s[42:43], 0, v2
	v_cndmask_b32_e64 v2, 0, 1, s[40:41]
	v_mfma_f32_16x16x32_f16 v[104:107], v[58:61], v[14:17], v[104:107]
	v_cmp_ne_u32_e32 vcc, 0, v2
	v_mov_b32_e32 v5, s42
	v_cmp_ngt_f32_e64 s[48:49], s70, v103
	v_mov_b32_e32 v2, vcc_lo
	v_cndmask_b32_e64 v2, v2, v5, s[38:39]
	v_mfma_f32_16x16x32_f16 v[108:111], v[54:57], v[18:21], v[104:107]
	v_lshrrev_b32_sdwa v2, v88, v2 dst_sel:DWORD dst_unused:UNUSED_PAD src0_sel:DWORD src1_sel:WORD_0
	v_and_b32_e32 v5, 1, v2
	v_cmp_eq_u32_e64 s[46:47], 0, v5
	v_and_b32_e32 v5, 2, v2
	v_cmp_eq_u32_e64 s[40:41], 0, v5
	v_and_b32_e32 v104, 4, v2
	v_and_b32_e32 v2, 8, v2
	s_nop 0
	v_cndmask_b32_e64 v107, v108, v71, s[46:47]
	v_cndmask_b32_e64 v105, v109, v71, s[40:41]
	v_cmp_eq_u32_e64 s[42:43], 0, v104
	v_cmp_eq_u32_e64 s[44:45], 0, v2
	v_max3_f32 v5, v107, s69, v105
	v_cndmask_b32_e64 v106, v110, v71, s[42:43]
	v_cndmask_b32_e64 v104, v111, v71, s[44:45]
	v_max3_f32 v2, v5, v106, v104
	ds_bpermute_b32 v5, v90, v2
	s_waitcnt lgkmcnt(0)
	v_max_f32_e32 v5, v5, v5
	v_max_f32_e32 v2, v2, v5
	ds_bpermute_b32 v5, v91, v2
	s_waitcnt lgkmcnt(0)
	v_max_f32_e32 v5, v5, v5
	v_max_f32_e32 v108, v2, v5
	v_sub_f32_e32 v2, v108, v103
	v_cmp_lt_f32_e32 vcc, s71, v2
	s_and_b64 vcc, s[48:49], vcc
	s_nop 0
	v_cndmask_b32_e64 v2, 0, 1, vcc
	v_cmp_ne_u32_e64 s[50:51], 0, v2
	s_cmp_lg_u64 s[50:51], 0
	s_cselect_b64 s[50:51], -1, 0
	s_cbranch_vccz .LBB0_117
	v_max_f32_e32 v2, v108, v108
	v_max_f32_e32 v5, v103, v103
	v_max_f32_e32 v5, v5, v2
	v_sub_f32_e32 v2, v103, v5
	v_exp_f32_e32 v2, v2
	s_cbranch_execnz .LBB0_100

.LBB0_102:
	v_sub_f32_e32 v105, v105, v5
	v_sub_f32_e32 v104, v104, v5
	v_exp_f32_e32 v105, v105
	v_exp_f32_e32 v104, v104
	v_sub_f32_e32 v103, v107, v5
	ds_write2_b64 v92, v[66:67], v[68:69] offset1:4
	ds_write2_b64 v92, v[62:63], v[64:65] offset0:8 offset1:12
	ds_read_b64_tr_b16 v[62:63], v93
	ds_read_b64_tr_b16 v[64:65], v93 offset:32
	v_cndmask_b32_e64 v107, v105, 0, s[40:41]
	v_cndmask_b32_e64 v108, v104, 0, s[44:45]
	ds_read_b64_tr_b16 v[68:69], v93 offset:64
	ds_read_b64_tr_b16 v[104:105], v93 offset:96
	ds_write2_b64 v92, v[58:59], v[60:61] offset1:4
	ds_write2_b64 v92, v[54:55], v[56:57] offset0:8 offset1:12
	ds_read_b64_tr_b16 v[54:55], v93
	v_sub_f32_e32 v106, v106, v5
	v_exp_f32_e32 v103, v103
	v_exp_f32_e32 v106, v106
	ds_read_b64_tr_b16 v[56:57], v93 offset:32
	ds_read_b64_tr_b16 v[58:59], v93 offset:64
	ds_read_b64_tr_b16 v[60:61], v93 offset:96
	v_cndmask_b32_e64 v103, v103, 0, s[46:47]
	v_cndmask_b32_e64 v106, v106, 0, s[42:43]
	v_cvt_pk_f16_f32 v67, v106, v108
	v_cvt_pk_f16_f32 v66, v103, v107
	s_waitcnt lgkmcnt(3)
	s_nop 0
	v_mfma_f32_16x16x16_f16 v[30:33], v[54:55], v[66:67], v[30:33]
	v_add_f32_e32 v54, 0, v103
	v_add_f32_e32 v54, v107, v54
	v_add_f32_e32 v54, v106, v54
	v_mfma_f32_16x16x16_f16 v[46:49], v[62:63], v[66:67], v[46:49]
	v_add_f32_e32 v54, v108, v54
	v_fmac_f32_e32 v54, v4, v2
	v_mfma_f32_16x16x16_f16 v[50:53], v[64:65], v[66:67], v[50:53]
	v_mfma_f32_16x16x16_f16 v[38:41], v[68:69], v[66:67], v[38:41]
	v_mfma_f32_16x16x16_f16 v[42:45], v[104:105], v[66:67], v[42:45]
	s_waitcnt lgkmcnt(2)
	v_mfma_f32_16x16x16_f16 v[34:37], v[56:57], v[66:67], v[34:37]
	s_waitcnt lgkmcnt(1)
	v_mfma_f32_16x16x16_f16 v[22:25], v[58:59], v[66:67], v[22:25]
	s_waitcnt lgkmcnt(0)
	v_mfma_f32_16x16x16_f16 v[26:29], v[60:61], v[66:67], v[26:29]
	s_and_saveexec_b64 s[40:41], s[0:1]
	s_cbranch_execz .LBB0_108
	ds_bpermute_b32 v2, v90, v54
	s_waitcnt vmcnt(5)
	v_mov_b32_e32 v99, v112
	v_mov_b32_e32 v100, v113
	v_mov_b32_e32 v101, v114
	v_mov_b32_e32 v102, v115
	s_waitcnt lgkmcnt(0)
	v_add_f32_e32 v54, v54, v2
	ds_bpermute_b32 v55, v91, v54
	s_lshl_b32 s95, s80, 1
	v_mov_b32_e32 v2, s95
	v_or_b32_e32 v4, 1, v2
	v_cmp_gt_i32_e32 vcc, s33, v4
	ds_read_b128 v[4:7], v86 offset:32768
	ds_read_b128 v[8:11], v86 offset:33792
	ds_read_b128 v[12:15], v86 offset:34816
	ds_read_b128 v[16:19], v86 offset:35840
	v_cvt_pk_f16_f32 v53, v52, v53
	v_cvt_pk_f16_f32 v52, v50, v51
	v_cvt_pk_f16_f32 v51, v48, v49
	v_cvt_pk_f16_f32 v50, v46, v47
	v_cvt_pk_f16_f32 v45, v44, v45
	v_cvt_pk_f16_f32 v44, v42, v43
	v_cvt_pk_f16_f32 v43, v40, v41
	v_cvt_pk_f16_f32 v42, v38, v39
	v_cvt_pk_f16_f32 v37, v36, v37
	v_cvt_pk_f16_f32 v36, v34, v35
	v_cvt_pk_f16_f32 v35, v32, v33
	v_cvt_pk_f16_f32 v34, v30, v31
	ds_read_b128 v[30:33], v86 offset:36864
	ds_read_b128 v[38:41], v86 offset:37888
	ds_read_b128 v[46:49], v86 offset:38912
	ds_read_b128 v[56:59], v86 offset:39936
	v_cvt_pk_f16_f32 v63, v28, v29
	v_cvt_pk_f16_f32 v62, v26, v27
	v_cvt_pk_f16_f32 v61, v24, v25
	v_cvt_pk_f16_f32 v60, v22, v23
	s_waitcnt lgkmcnt(7)
	v_mfma_f32_16x16x32_f16 v[4:7], v[4:7], v[50:53], 0
	s_waitcnt lgkmcnt(6)
	v_mfma_f32_16x16x32_f16 v[4:7], v[8:11], v[42:45], v[4:7]
	s_waitcnt lgkmcnt(5)
	v_mfma_f32_16x16x32_f16 v[4:7], v[12:15], v[34:37], v[4:7]
	s_waitcnt lgkmcnt(4)
	v_mfma_f32_16x16x32_f16 v[12:15], v[16:19], v[60:63], v[4:7]
	ds_read_b128 v[8:11], v86 offset:44032
	ds_read_b128 v[16:19], v86 offset:43008
	ds_read_b128 v[20:23], v86 offset:41984
	ds_read_b128 v[24:27], v86 offset:40960
	s_waitcnt lgkmcnt(7)
	v_mfma_f32_16x16x32_f16 v[4:7], v[30:33], v[50:53], 0
	s_waitcnt lgkmcnt(6)
	v_mfma_f32_16x16x32_f16 v[4:7], v[38:41], v[42:45], v[4:7]
	s_waitcnt lgkmcnt(5)
	v_mfma_f32_16x16x32_f16 v[4:7], v[46:49], v[34:37], v[4:7]
	s_waitcnt lgkmcnt(4)
	v_mfma_f32_16x16x32_f16 v[4:7], v[56:59], v[60:63], v[4:7]
	ds_read_b128 v[28:31], v86 offset:45056
	ds_read_b128 v[38:41], v86 offset:46080
	ds_read_b128 v[46:49], v86 offset:47104
	ds_read_b128 v[56:59], v86 offset:48128
	s_waitcnt lgkmcnt(4)
	v_mfma_f32_16x16x32_f16 v[24:27], v[24:27], v[50:53], 0
	v_mfma_f32_16x16x32_f16 v[20:23], v[20:23], v[42:45], v[24:27]
	v_mfma_f32_16x16x32_f16 v[16:19], v[16:19], v[34:37], v[20:23]
	v_mfma_f32_16x16x32_f16 v[8:11], v[8:11], v[60:63], v[16:19]
	s_nop 5
	ds_read_b128 v[20:23], v86 offset:52224
	ds_read_b128 v[24:27], v86 offset:51200
	ds_read_b128 v[64:67], v86 offset:50176
	ds_read_b128 v[104:107], v86 offset:49152
	s_waitcnt lgkmcnt(7)
	v_mfma_f32_16x16x32_f16 v[16:19], v[28:31], v[50:53], 0
	s_waitcnt lgkmcnt(6)
	v_mfma_f32_16x16x32_f16 v[16:19], v[38:41], v[42:45], v[16:19]
	s_waitcnt lgkmcnt(5)
	v_mfma_f32_16x16x32_f16 v[16:19], v[46:49], v[34:37], v[16:19]
	s_waitcnt lgkmcnt(4)
	v_mfma_f32_16x16x32_f16 v[16:19], v[56:59], v[60:63], v[16:19]
	ds_read_b128 v[28:31], v86 offset:53248
	ds_read_b128 v[38:41], v86 offset:54272
	ds_read_b128 v[46:49], v86 offset:55296
	ds_read_b128 v[56:59], v86 offset:56320
	s_waitcnt lgkmcnt(4)
	v_mfma_f32_16x16x32_f16 v[104:107], v[104:107], v[50:53], 0
	v_mfma_f32_16x16x32_f16 v[64:67], v[64:67], v[42:45], v[104:107]
	v_mfma_f32_16x16x32_f16 v[24:27], v[24:27], v[34:37], v[64:67]
	v_mfma_f32_16x16x32_f16 v[20:23], v[20:23], v[60:63], v[24:27]
	s_nop 5
	ds_read_b128 v[64:67], v86 offset:60416
	ds_read_b128 v[104:107], v86 offset:59392
	ds_read_b128 v[108:111], v86 offset:58368
	ds_read_b128 v[112:115], v86 offset:57344
	s_waitcnt lgkmcnt(7)
	v_mfma_f32_16x16x32_f16 v[24:27], v[28:31], v[50:53], 0
	s_waitcnt lgkmcnt(6)
	v_mfma_f32_16x16x32_f16 v[24:27], v[38:41], v[42:45], v[24:27]
	s_waitcnt lgkmcnt(5)
	v_mfma_f32_16x16x32_f16 v[24:27], v[46:49], v[34:37], v[24:27]
	s_waitcnt lgkmcnt(4)
	v_mfma_f32_16x16x32_f16 v[24:27], v[56:59], v[60:63], v[24:27]
	ds_read_b128 v[38:41], v86 offset:61440
	ds_read_b128 v[46:49], v86 offset:62464
	ds_read_b128 v[56:59], v86 offset:63488
	ds_read_b128 v[116:119], v86 offset:64512
	s_waitcnt lgkmcnt(4)
	v_mfma_f32_16x16x32_f16 v[28:31], v[112:115], v[50:53], 0
	v_mfma_f32_16x16x32_f16 v[28:31], v[108:111], v[42:45], v[28:31]
	v_mfma_f32_16x16x32_f16 v[28:31], v[104:107], v[34:37], v[28:31]
	v_mfma_f32_16x16x32_f16 v[28:31], v[64:67], v[60:63], v[28:31]
	s_waitcnt lgkmcnt(3)
	v_mfma_f32_16x16x32_f16 v[38:41], v[38:41], v[50:53], 0
	s_waitcnt lgkmcnt(2)
	v_mfma_f32_16x16x32_f16 v[38:41], v[46:49], v[42:45], v[38:41]
	s_waitcnt lgkmcnt(1)
	v_mfma_f32_16x16x32_f16 v[32:35], v[56:59], v[34:37], v[38:41]
	s_waitcnt lgkmcnt(0)
	v_mfma_f32_16x16x32_f16 v[32:35], v[116:119], v[60:63], v[32:35]
	s_or_b64 s[42:43], s[38:39], vcc
	s_and_saveexec_b64 s[0:1], s[42:43]
	s_cbranch_execz .LBB0_105
	v_lshlrev_b32_e32 v36, 1, v78
	ds_read_b128 v[36:39], v36 offset:27472
	v_cndmask_b32_e64 v12, 0, v12, s[14:15]
	v_cndmask_b32_e64 v13, 0, v13, s[14:15]
	v_cndmask_b32_e64 v14, 0, v14, s[14:15]
	v_cndmask_b32_e64 v15, 0, v15, s[14:15]
	v_cndmask_b32_e64 v7, v15, v7, s[12:13]
	v_cndmask_b32_e64 v6, v14, v6, s[12:13]
	v_cndmask_b32_e64 v5, v13, v5, s[12:13]
	v_cndmask_b32_e64 v4, v12, v4, s[12:13]
	v_add_f32_e32 v40, v54, v55
	v_cndmask_b32_e64 v4, v4, v8, s[10:11]
	v_cndmask_b32_e64 v5, v5, v9, s[10:11]
	v_cndmask_b32_e64 v6, v6, v10, s[10:11]
	v_cndmask_b32_e64 v7, v7, v11, s[10:11]
	v_rcp_f32_e32 v12, v40
	v_cndmask_b32_e64 v7, v7, v19, s[8:9]
	v_cndmask_b32_e64 v6, v6, v18, s[8:9]
	v_cndmask_b32_e64 v5, v5, v17, s[8:9]
	v_cndmask_b32_e64 v4, v4, v16, s[8:9]
	v_cndmask_b32_e64 v4, v4, v20, s[6:7]
	v_cndmask_b32_e64 v5, v5, v21, s[6:7]
	v_cndmask_b32_e64 v6, v6, v22, s[6:7]
	v_cndmask_b32_e64 v7, v7, v23, s[6:7]
	v_cndmask_b32_e64 v7, v7, v27, s[20:21]
	v_cndmask_b32_e64 v6, v6, v26, s[20:21]
	v_cndmask_b32_e64 v5, v5, v25, s[20:21]
	v_cndmask_b32_e64 v4, v4, v24, s[20:21]
	v_cmp_lt_f32_e32 vcc, 0, v40
	v_cndmask_b32_e64 v4, v4, v28, s[18:19]
	v_cndmask_b32_e64 v5, v5, v29, s[18:19]
	v_cndmask_b32_e64 v6, v6, v30, s[18:19]
	v_cndmask_b32_e64 v7, v7, v31, s[18:19]
	v_cndmask_b32_e32 v8, 0, v12, vcc
	v_cndmask_b32_e64 v7, v7, v35, s[16:17]
	v_cndmask_b32_e64 v6, v6, v34, s[16:17]
	v_cndmask_b32_e64 v5, v5, v33, s[16:17]
	v_cndmask_b32_e64 v4, v4, v32, s[16:17]
	v_or_b32_e32 v2, v2, v89
	s_waitcnt lgkmcnt(0)
	v_fma_mixlo_f16 v4, v8, v4, v36
	v_fma_mixlo_f16 v5, v8, v5, v37
	v_fma_mixlo_f16 v6, v8, v6, v38
	v_fma_mixlo_f16 v7, v8, v7, v39
	v_cndmask_b32_e32 v4, 0, v4, vcc
	v_cndmask_b32_e32 v8, 0, v5, vcc
	v_cndmask_b32_e32 v5, 0, v6, vcc
	v_cndmask_b32_e32 v6, 0, v7, vcc
	v_pack_b32_f16 v5, v5, v6
	v_pack_b32_f16 v4, v4, v8
	v_mad_u64_u32 v[6:7], s[42:43], v2, s72, v[78:79]
	ds_write_b64 v6, v[4:5]
.LBB0_105:
	s_or_b64 exec, exec, s[0:1]
	v_mov_b32_e32 v4, v3
	v_mov_b32_e32 v5, v3
	v_mov_b32_e32 v2, v3
	v_mov_b64_e32 v[8:9], v[4:5]
	v_mov_b64_e32 v[12:13], v[4:5]
	v_mov_b64_e32 v[16:17], v[4:5]
	v_mov_b64_e32 v[20:21], v[4:5]
	v_mov_b64_e32 v[6:7], v[2:3]
	v_mov_b64_e32 v[10:11], v[2:3]
	v_mov_b64_e32 v[14:15], v[2:3]
	v_mov_b64_e32 v[18:19], v[2:3]
	s_and_saveexec_b64 s[0:1], s[78:79]
	s_cbranch_execz .LBB0_107
	ds_read_b128 v[4:7], v86
	ds_read_b128 v[8:11], v86 offset:1024
	ds_read_b128 v[12:15], v86 offset:4096
	ds_read_b128 v[22:25], v86 offset:5120
	ds_read_b128 v[34:37], v86 offset:2048
	ds_read_b128 v[38:41], v86 offset:3072
	ds_read_b128 v[42:45], v86 offset:6144
	ds_read_b128 v[46:49], v86 offset:7168
	v_cndmask_b32_e64 v21, 0, v102, s[22:23]
	v_cndmask_b32_e64 v20, 0, v101, s[22:23]
	v_cndmask_b32_e64 v19, 0, v100, s[22:23]
	v_cndmask_b32_e64 v18, 0, v99, s[22:23]
	v_cndmask_b32_e64 v29, 0, v102, s[24:25]
	v_cndmask_b32_e64 v28, 0, v101, s[24:25]
	v_cndmask_b32_e64 v27, 0, v100, s[24:25]
	v_cndmask_b32_e64 v26, 0, v99, s[24:25]
	v_cndmask_b32_e64 v33, 0, v102, s[26:27]
	v_cndmask_b32_e64 v32, 0, v101, s[26:27]
	v_cndmask_b32_e64 v31, 0, v100, s[26:27]
	v_cndmask_b32_e64 v30, 0, v99, s[26:27]
	v_cndmask_b32_e64 v53, 0, v102, s[28:29]
	v_cndmask_b32_e64 v52, 0, v101, s[28:29]
	v_cndmask_b32_e64 v51, 0, v100, s[28:29]
	v_cndmask_b32_e64 v50, 0, v99, s[28:29]
	s_waitcnt lgkmcnt(7)
	v_mfma_f32_16x16x32_f16 v[4:7], v[4:7], v[18:21], 0
	s_waitcnt lgkmcnt(5)
	v_mfma_f32_16x16x32_f16 v[12:15], v[12:15], v[18:21], 0
	v_mfma_f32_16x16x32_f16 v[4:7], v[8:11], v[26:29], v[4:7]
	s_waitcnt lgkmcnt(4)
	v_mfma_f32_16x16x32_f16 v[8:11], v[22:25], v[26:29], v[12:15]
	s_nop 4
	ds_read_b128 v[12:15], v86 offset:13312
	ds_read_b128 v[22:25], v86 offset:12288
	ds_read_b128 v[54:57], v86 offset:9216
	ds_read_b128 v[58:61], v86 offset:8192
	s_waitcnt lgkmcnt(7)
	v_mfma_f32_16x16x32_f16 v[4:7], v[34:37], v[30:33], v[4:7]
	s_waitcnt lgkmcnt(5)
	v_mfma_f32_16x16x32_f16 v[8:11], v[42:45], v[30:33], v[8:11]
	s_waitcnt lgkmcnt(4)
	v_mfma_f32_16x16x32_f16 v[34:37], v[46:49], v[50:53], v[8:11]
	v_mfma_f32_16x16x32_f16 v[4:7], v[38:41], v[50:53], v[4:7]
	s_nop 6
	v_cvt_pk_f16_f32 v9, v36, v37
	v_cvt_pk_f16_f32 v8, v34, v35
	v_cvt_pk_f16_f32 v7, v6, v7
	v_cvt_pk_f16_f32 v6, v4, v5
	ds_read_b128 v[34:37], v86 offset:10240
	ds_read_b128 v[38:41], v86 offset:11264
	ds_read_b128 v[42:45], v86 offset:14336
	ds_read_b128 v[46:49], v86 offset:15360
	s_waitcnt lgkmcnt(6)
	v_mfma_f32_16x16x32_f16 v[22:25], v[22:25], v[18:21], 0
	s_waitcnt lgkmcnt(4)
	v_mfma_f32_16x16x32_f16 v[58:61], v[58:61], v[18:21], 0
	v_mfma_f32_16x16x32_f16 v[10:13], v[12:15], v[26:29], v[22:25]
	v_mfma_f32_16x16x32_f16 v[54:57], v[54:57], v[26:29], v[58:61]
	ds_read_b128 v[14:17], v86 offset:21504
	s_nop 2
	ds_read_b128 v[22:25], v86 offset:20480
	s_nop 0
	ds_read_b128 v[58:61], v86 offset:17408
	ds_read_b128 v[62:65], v86 offset:16384
	s_waitcnt lgkmcnt(7)
	v_mfma_f32_16x16x32_f16 v[34:37], v[34:37], v[30:33], v[54:57]
	s_waitcnt lgkmcnt(5)
	v_mfma_f32_16x16x32_f16 v[10:13], v[42:45], v[30:33], v[10:13]
	s_waitcnt lgkmcnt(4)
	v_mfma_f32_16x16x32_f16 v[10:13], v[46:49], v[50:53], v[10:13]
	v_mfma_f32_16x16x32_f16 v[34:37], v[38:41], v[50:53], v[34:37]
	s_nop 6
	v_cvt_pk_f16_f32 v13, v12, v13
	v_cvt_pk_f16_f32 v12, v10, v11
	v_cvt_pk_f16_f32 v11, v36, v37
	v_cvt_pk_f16_f32 v10, v34, v35
	ds_read_b128 v[34:37], v86 offset:18432
	ds_read_b128 v[38:41], v86 offset:19456
	ds_read_b128 v[42:45], v86 offset:22528
	ds_read_b128 v[46:49], v86 offset:23552
	s_waitcnt lgkmcnt(6)
	v_mfma_f32_16x16x32_f16 v[22:25], v[22:25], v[18:21], 0
	s_waitcnt lgkmcnt(4)
	v_mfma_f32_16x16x32_f16 v[54:57], v[62:65], v[18:21], 0
	v_mfma_f32_16x16x32_f16 v[14:17], v[14:17], v[26:29], v[22:25]
	v_mfma_f32_16x16x32_f16 v[54:57], v[58:61], v[26:29], v[54:57]
	s_nop 3
	ds_read_b128 v[22:25], v86 offset:29696
	ds_read_b128 v[58:61], v86 offset:28672
	ds_read_b128 v[62:65], v86 offset:25600
	ds_read_b128 v[66:69], v86 offset:24576
	s_waitcnt lgkmcnt(7)
	v_mfma_f32_16x16x32_f16 v[34:37], v[34:37], v[30:33], v[54:57]
	s_waitcnt lgkmcnt(5)
	v_mfma_f32_16x16x32_f16 v[14:17], v[42:45], v[30:33], v[14:17]
	s_waitcnt lgkmcnt(4)
	v_mfma_f32_16x16x32_f16 v[14:17], v[46:49], v[50:53], v[14:17]
	v_mfma_f32_16x16x32_f16 v[34:37], v[38:41], v[50:53], v[34:37]
	s_nop 6
	v_cvt_pk_f16_f32 v17, v16, v17
	v_cvt_pk_f16_f32 v16, v14, v15
	v_cvt_pk_f16_f32 v15, v36, v37
	v_cvt_pk_f16_f32 v14, v34, v35
	ds_read_b128 v[34:37], v86 offset:26624
	ds_read_b128 v[38:41], v86 offset:27648
	ds_read_b128 v[42:45], v86 offset:30720
	ds_read_b128 v[46:49], v86 offset:31744
	s_waitcnt lgkmcnt(4)
	v_mfma_f32_16x16x32_f16 v[54:57], v[66:69], v[18:21], 0
	v_mfma_f32_16x16x32_f16 v[18:21], v[58:61], v[18:21], 0
	v_mfma_f32_16x16x32_f16 v[18:21], v[22:25], v[26:29], v[18:21]
	v_mfma_f32_16x16x32_f16 v[54:57], v[62:65], v[26:29], v[54:57]
	s_waitcnt lgkmcnt(3)
	v_mfma_f32_16x16x32_f16 v[22:25], v[34:37], v[30:33], v[54:57]
	s_waitcnt lgkmcnt(1)
	v_mfma_f32_16x16x32_f16 v[18:21], v[42:45], v[30:33], v[18:21]
	s_waitcnt lgkmcnt(0)
	v_mfma_f32_16x16x32_f16 v[18:21], v[46:49], v[50:53], v[18:21]
	v_mfma_f32_16x16x32_f16 v[22:25], v[38:41], v[50:53], v[22:25]
	s_nop 6
	v_cvt_pk_f16_f32 v21, v20, v21
	v_cvt_pk_f16_f32 v20, v18, v19
	v_cvt_pk_f16_f32 v19, v24, v25
	v_cvt_pk_f16_f32 v18, v22, v23

.LBB0_108:
	s_or_b64 exec, exec, s[40:41]
	s_and_b64 s[0:1], exec, s[36:37]
	s_or_b64 s[62:63], s[0:1], s[62:63]
	v_mov_b32_e32 v103, v5
	v_mov_b32_e32 v4, v54
	v_mov_b32_e32 v2, v83
	v_mov_b32_e32 v56, v81
	v_mov_b32_e32 v57, v84
	v_mov_b32_e32 v54, v87
	s_and_saveexec_b64 s[0:1], s[34:35]
	s_cbranch_execz .LBB0_94
	v_add_u32_e32 v57, 1, v84
	v_lshlrev_b32_e32 v2, 4, v57
	v_cmp_ge_i32_e32 vcc, v2, v83
	v_mov_b32_e32 v54, v87
	v_mov_b32_e32 v56, v81
	v_mov_b32_e32 v2, v83
	s_and_saveexec_b64 s[34:35], vcc
	s_cbranch_execz .LBB0_93
	v_mov_b32_e32 v2, 0
	s_and_saveexec_b64 s[36:37], s[2:3]
	s_cbranch_execz .LBB0_114
	s_mov_b64 s[42:43], exec
	v_mbcnt_lo_u32_b32 v2, s42, 0
	v_mbcnt_hi_u32_b32 v2, s43, v2
	v_cmp_eq_u32_e32 vcc, 0, v2
	s_and_saveexec_b64 s[40:41], vcc
	s_bcnt1_i32_b64 s42, s[42:43]
	v_mov_b32_e32 v5, s42
	v_mov_b32_e32 v56, 0x26b40
	ds_add_rtn_u32 v5, v56, v5
	s_or_b64 exec, exec, s[40:41]
	s_waitcnt lgkmcnt(0)
	v_readfirstlane_b32 s40, v5
	s_nop 1
	v_add_u32_e32 v2, s40, v2
.LBB0_114:
	s_or_b64 exec, exec, s[36:37]
	v_readfirstlane_b32 s42, v2
	v_cmp_gt_i32_e32 vcc, s68, v82
	v_mov_b32_e32 v56, v81
	v_mov_b32_e32 v2, v83
	s_and_saveexec_b64 s[36:37], vcc
	s_cbranch_execz .LBB0_92
	v_lshlrev_b32_e32 v2, 1, v82
	v_min_i32_e32 v5, s67, v2
	v_lshl_add_u32 v5, v5, 3, s77
	ds_read_b64 v[54:55], v5
	v_or_b32_e32 v5, 1, v2
	v_cmp_gt_i32_e32 vcc, s33, v5
	v_mov_b32_e32 v5, 0
	s_waitcnt lgkmcnt(0)
	v_readfirstlane_b32 s43, v54
	v_readfirstlane_b32 s44, v55
	s_and_saveexec_b64 s[40:41], vcc
	s_cbranch_execz .LBB0_91
	v_lshl_add_u32 v2, v2, 3, s73
	ds_read_b32 v2, v2
	s_waitcnt lgkmcnt(0)
	v_readfirstlane_b32 s45, v2
	s_nop 1
	v_mov_b32_e32 v5, s45
	s_branch .LBB0_91
.Lattn_skip:
	v_mov_b32_e32 v5, v103
	v_mov_b32_e32 v54, v4
	s_mov_b64 s[40:41], exec
	s_branch .LBB0_108

	.amdhsa_kernel _Z7k_attn3PKDF16_S0_PKiS2_PiPKDv8_DF16_PKfS6_S8_Pf
		.amdhsa_group_segment_fixed_size 159056
		.amdhsa_private_segment_fixed_size 0
		.amdhsa_kernarg_size 80
		.amdhsa_user_sgpr_count 2
		.amdhsa_user_sgpr_dispatch_ptr 0
		.amdhsa_user_sgpr_queue_ptr 0
		.amdhsa_user_sgpr_kernarg_segment_ptr 1
		.amdhsa_user_sgpr_dispatch_id 0
		.amdhsa_user_sgpr_kernarg_preload_length 0
		.amdhsa_user_sgpr_kernarg_preload_offset 0
		.amdhsa_user_sgpr_private_segment_size 0
		.amdhsa_uses_dynamic_stack 0
		.amdhsa_enable_private_segment 0
		.amdhsa_system_sgpr_workgroup_id_x 1
		.amdhsa_system_sgpr_workgroup_id_y 0
		.amdhsa_system_sgpr_workgroup_id_z 0
		.amdhsa_system_sgpr_workgroup_info 0
		.amdhsa_system_vgpr_workitem_id 0
		.amdhsa_next_free_vgpr 128
		.amdhsa_next_free_sgpr 96
		.amdhsa_accum_offset 128
		.amdhsa_reserve_vcc 1
		.amdhsa_float_round_mode_32 0
		.amdhsa_float_round_mode_16_64 0
		.amdhsa_float_denorm_mode_32 3
		.amdhsa_float_denorm_mode_16_64 3
		.amdhsa_dx10_clamp 1
		.amdhsa_ieee_mode 1
		.amdhsa_fp16_overflow 0
		.amdhsa_tg_split 0
		.amdhsa_exception_fp_ieee_invalid_op 0
		.amdhsa_exception_fp_denorm_src 0
		.amdhsa_exception_fp_ieee_div_zero 0
		.amdhsa_exception_fp_ieee_overflow 0
		.amdhsa_exception_fp_ieee_underflow 0
		.amdhsa_exception_fp_ieee_inexact 0
		.amdhsa_exception_int_div_zero 0
	.end_amdhsa_kernel

amdhsa.kernels:
  - .agpr_count:     0
    .args:
      - .actual_access:  read_only
        .address_space:  global
        .offset:         0
        .size:           8
        .value_kind:     global_buffer
      - .actual_access:  read_only
        .address_space:  global
        .offset:         8
        .size:           8
        .value_kind:     global_buffer
      - .actual_access:  read_only
        .address_space:  global
        .offset:         16
        .size:           8
        .value_kind:     global_buffer
      - .actual_access:  read_only
        .address_space:  global
        .offset:         24
        .size:           8
        .value_kind:     global_buffer
      - .address_space:  global
        .offset:         32
        .size:           8
        .value_kind:     global_buffer
      - .actual_access:  read_only
        .address_space:  global
        .offset:         40
        .size:           8
        .value_kind:     global_buffer
      - .actual_access:  read_only
        .address_space:  global
        .offset:         48
        .size:           8
        .value_kind:     global_buffer
      - .actual_access:  read_only
        .address_space:  global
        .offset:         56
        .size:           8
        .value_kind:     global_buffer
      - .actual_access:  read_only
        .address_space:  global
        .offset:         64
        .size:           8
        .value_kind:     global_buffer
      - .actual_access:  write_only
        .address_space:  global
        .offset:         72
        .size:           8
        .value_kind:     global_buffer
    .group_segment_fixed_size: 159056
    .kernarg_segment_align: 8
    .kernarg_segment_size: 80
    .language:       OpenCL C
    .language_version:
      - 2
      - 0
    .max_flat_workgroup_size: 1024
    .name:           _Z7k_attn3PKDF16_S0_PKiS2_PiPKDv8_DF16_PKfS6_S8_Pf
    .private_segment_fixed_size: 0
    .sgpr_count:     79
    .sgpr_spill_count: 0
    .symbol:         _Z7k_attn3PKDF16_S0_PKiS2_PiPKDv8_DF16_PKfS6_S8_Pf.kd
    .uniform_work_group_size: 1
    .uses_dynamic_stack: false
    .vgpr_count:     128
    .vgpr_spill_count: 0
    .wavefront_size: 64
  - .agpr_count:     0
    .args:
      - .actual_access:  read_only
        .address_space:  global
        .offset:         0
        .size:           8
        .value_kind:     global_buffer
      - .actual_access:  write_only
        .address_space:  global
        .offset:         8
        .size:           8
        .value_kind:     global_buffer
      - .actual_access:  read_only
        .address_space:  global
        .offset:         16
        .size:           8
        .value_kind:     global_buffer
      - .actual_access:  read_only
        .address_space:  global
        .offset:         24
        .size:           8
        .value_kind:     global_buffer
      - .actual_access:  read_only
        .address_space:  global
        .offset:         32
        .size:           8
        .value_kind:     global_buffer
      - .actual_access:  read_only
        .address_space:  global
        .offset:         40
        .size:           8
        .value_kind:     global_buffer
      - .actual_access:  read_only
        .address_space:  global
        .offset:         48
        .size:           8
        .value_kind:     global_buffer
      - .actual_access:  read_only
        .address_space:  global
        .offset:         56
        .size:           8
        .value_kind:     global_buffer
      - .actual_access:  read_only
        .address_space:  global
        .offset:         64
        .size:           8
        .value_kind:     global_buffer
      - .actual_access:  write_only
        .address_space:  global
        .offset:         72
        .size:           8
        .value_kind:     global_buffer
      - .actual_access:  write_only
        .address_space:  global
        .offset:         80
        .size:           8
        .value_kind:     global_buffer
      - .actual_access:  write_only
        .address_space:  global
        .offset:         88
        .size:           8
        .value_kind:     global_buffer
      - .actual_access:  write_only
        .address_space:  global
        .offset:         96
        .size:           8
        .value_kind:     global_buffer
    .group_segment_fixed_size: 1024
    .kernarg_segment_align: 8
    .kernarg_segment_size: 104
    .language:       OpenCL C
    .language_version:
      - 2
      - 0
    .max_flat_workgroup_size: 512
    .name:           _Z4k_l1PK15HIP_vector_typeIiLj4EEPiPKfS5_S5_S5_S5_S5_S5_PDF16_PfS6_S6_
    .private_segment_fixed_size: 0
    .sgpr_count:     22
    .sgpr_spill_count: 0
    .symbol:         _Z4k_l1PK15HIP_vector_typeIiLj4EEPiPKfS5_S5_S5_S5_S5_S5_PDF16_PfS6_S6_.kd
    .uniform_work_group_size: 1
    .uses_dynamic_stack: false
    .vgpr_count:     24
    .vgpr_spill_count: 0
    .wavefront_size: 64
  - .agpr_count:     0
    .args:
      - .actual_access:  read_only
        .address_space:  global
        .offset:         0
        .size:           8
        .value_kind:     global_buffer
      - .actual_access:  read_only
        .address_space:  global
        .offset:         8
        .size:           8
        .value_kind:     global_buffer
      - .actual_access:  read_only
        .address_space:  global
        .offset:         16
        .size:           8
        .value_kind:     global_buffer
      - .actual_access:  write_only
        .address_space:  global
        .offset:         24
        .size:           8
        .value_kind:     global_buffer
      - .actual_access:  write_only
        .address_space:  global
        .offset:         32
        .size:           8
        .value_kind:     global_buffer
      - .actual_access:  read_only
        .address_space:  global
        .offset:         40
        .size:           8
        .value_kind:     global_buffer
      - .actual_access:  read_only
        .address_space:  global
        .offset:         48
        .size:           8
        .value_kind:     global_buffer
      - .actual_access:  read_only
        .address_space:  global
        .offset:         56
        .size:           8
        .value_kind:     global_buffer
      - .actual_access:  write_only
        .address_space:  global
        .offset:         64
        .size:           8
        .value_kind:     global_buffer
      - .actual_access:  write_only
        .address_space:  global
        .offset:         72
        .size:           8
        .value_kind:     global_buffer
    .group_segment_fixed_size: 53248
    .kernarg_segment_align: 8
    .kernarg_segment_size: 80
    .language:       OpenCL C
    .language_version:
      - 2
      - 0
    .max_flat_workgroup_size: 512
    .name:           _Z4k_l2PK15HIP_vector_typeIiLj4EES2_PKiPiS5_PKfPKDv8_DF16_S7_PDF16_SB_
    .private_segment_fixed_size: 0
    .sgpr_count:     34
    .sgpr_spill_count: 0
    .symbol:         _Z4k_l2PK15HIP_vector_typeIiLj4EES2_PKiPiS5_PKfPKDv8_DF16_S7_PDF16_SB_.kd
    .uniform_work_group_size: 1
    .uses_dynamic_stack: false
    .vgpr_count:     126
    .vgpr_spill_count: 0
    .wavefront_size: 64
